# gate_up SwiGLU epilogue rewritten by hand: 6 VALU per output (rf^2 folded into the rcp argument), no v_mov/s_nop padding, row factors prefetched; f32 math
# baseline (speedup 1.0000x reference)
; #define PG8_LAS __attribute__((address_space(3)))
; #define PG8_STAGE(bufoff, gbase, voff) do { _Pragma("unroll") for (int _i = 0; _i < 2; ++_i) \
;         __builtin_amdgcn_global_load_lds((const unsigned*)((const char*)(gbase) + (voff)[_i]), (PG8_LAS unsigned*)(lds + (bufoff) + ldsw + _i * 8192), 16, 0, 0); } while (0)
; #define PG8_WAIT_V(n) asm volatile("s_waitcnt vmcnt(" #n ")" ::: "memory")
; #define PG8_BAR __builtin_amdgcn_s_barrier()
; template <class Epi, class Sched, bool ALIGN_EPI = false, bool SP2 = false>
; __device__ __forceinline__ void gemm_phase(PG8_LAS unsigned char* lds, const Gemm g, const Sched& S, const Epi& E) {
;     ...
;         PG8_WAIT_V(2); PG8_BAR;
;         if constexpr (Epi::ROWSCALE) stage_row_factors(rowp_, (PG8_LAS float*)E.rsl, tid);
;         PG8_STAGE(PG8_SB(1, 0), cB + kstep, voffB); PG8_STAGE(PG8_SA(1, 0), cA + kstep, voffA); PG8_STAGE(PG8_SB(1, 1), cB + hstep + kstep, voffB);
;         PG8_WAIT_V(6); PG8_BAR;
.LBB0_389:
	s_or_b64 exec, exec, s[6:7]
	s_add_u32 s35, s16, 0x500000
	s_addc_u32 s40, s17, 0
	s_and_b32 s12, s11, 3
	s_add_i32 m0, s19, 0x18000
	s_waitcnt vmcnt(0)
	v_lshl_add_u64 v[4:5], v[12:13], 0, s[42:43]
	s_lshl_b32 s6, s26, 13
	s_lshl_b32 s7, s12, 12
	global_load_lds_dwordx4 v[4:5], off
	v_lshl_add_u64 v[4:5], v[14:15], 0, s[42:43]
	s_add_i32 m0, s19, 0x1a000
	s_add_i32 s41, s19, 0x8000
	s_add_i32 s71, s19, 0xa000
	global_load_lds_dwordx4 v[4:5], off
	v_lshl_add_u64 v[4:5], v[10:11], 0, s[42:43]
	s_mov_b32 m0, s41
	s_add_u32 s4, s0, 0x40080
	global_load_lds_dwordx4 v[4:5], off
	v_lshl_add_u64 v[4:5], v[8:9], 0, s[42:43]
	s_mov_b32 m0, s71
	s_addc_u32 s5, s1, 0
	global_load_lds_dwordx4 v[4:5], off
	s_add_i32 m0, s19, 0x1c000
	v_lshl_add_u64 v[4:5], s[4:5], 0, v[166:167]
	global_load_lds_dwordx4 v[4:5], off
	v_lshl_add_u64 v[4:5], s[4:5], 0, v[170:171]
	s_add_i32 m0, s19, 0x1e000
	s_cmpk_lt_u32 s10, 0x100
	global_load_lds_dwordx4 v[4:5], off
	v_and_b32_e32 v4, 15, v2
	v_bfe_u32 v5, v2, 4, 2
	v_lshl_or_b32 v202, s26, 6, v4
	v_lshlrev_b32_e32 v7, 4, v5
	v_lshlrev_b32_e32 v8, 2, v202
	v_lshlrev_b32_e32 v2, 2, v2
	v_lshl_or_b32 v7, v4, 6, v7
	v_and_b32_e32 v9, 32, v8
	v_and_b32_e32 v2, 32, v2
	v_bitop3_b32 v9, v7, s6, v9 bitop3:0xde
	v_bitop3_b32 v203, v7, s7, v2 bitop3:0xde
	s_cselect_b64 s[58:59], -1, 0
	s_lshl_b32 s6, s11, 4
	v_lshlrev_b32_e32 v2, 2, v5
	v_and_or_b32 v204, s6, 16, v2
	s_lshl_b32 s10, s12, 1
	s_or_b32 s74, s10, -16
	s_add_i32 s10, 0, 0x20400
	v_lshlrev_b32_e32 v2, 2, v204
	v_lshlrev_b32_e32 v6, 3, v5
	v_cmp_eq_u32_e64 s[4:5], 0, v5
	s_bfe_u32 s73, s11, 0x10001
	v_cmp_eq_u32_e64 s[6:7], 0, v4
	v_add_u32_e32 v205, s10, v8
	v_lshl_add_u64 v[4:5], s[16:17], 0, v[2:3]
	s_mov_b64 s[10:11], 0x100000
	v_lshlrev_b32_e32 v2, 14, v16
	v_lshl_add_u64 v[174:175], v[4:5], 0, s[10:11]
	s_mov_b64 s[10:11], 0x300000
	v_and_b32_e32 v2, 0xffff8000, v2
	v_lshl_add_u64 v[176:177], v[4:5], 0, s[10:11]
	v_lshl_add_u32 v2, v17, 11, v2
	v_and_b32_e32 v4, 1, v16
	v_lshl_or_b32 v2, v4, 6, v2
	v_lshl_add_u32 v178, v18, 1, v2
	v_lshlrev_b32_e32 v2, 14, v19
	v_and_b32_e32 v2, 0xffff8000, v2
	s_waitcnt vmcnt(6)
	v_lshl_add_u32 v2, v20, 11, v2
	v_and_b32_e32 v4, 1, v19
	s_add_u32 s75, s16, 0xf000000
	v_lshl_or_b32 v2, v4, 6, v2
	v_lshl_or_b32 v172, s12, 5, v6
	v_mov_b32_e32 v173, v3
	s_mov_b32 s72, 0
	s_addc_u32 s76, s17, 0
	v_mov_b32_e32 v179, v3
	v_lshl_add_u32 v180, v21, 1, v2
	v_mov_b32_e32 v181, v3
	v_add_u32_e32 v206, 0, v9
	s_barrier
	s_branch .LBB0_392

; #define PG8_LAS __attribute__((address_space(3)))
; __device__ __forceinline__ float sigm(float x) { return __builtin_amdgcn_rcpf(1.0f + __builtin_amdgcn_exp2f(-1.4426950408889634f * x)); }
; __device__ __forceinline__ u32x4 pack8(const f32x4 a, const f32x4 b) { u32x4 w; w.x = cvt_pk_bf16(a[0], a[1]); w.y = cvt_pk_bf16(a[2], a[3]); w.z = cvt_pk_bf16(b[0], b[1]); w.w = cvt_pk_bf16(b[2], b[3]); return w; }
;     __device__ __forceinline__ void operator()(const f32x4 (&acc)[2][2][4][2], const Unit& u, int wr, int wc, int fr, int fq) const {
;         const int rl0 = wr * 64 + fr + (u.half == 2 ? HALF : 0), row0 = u.pm * BM + rl0, col0 = u.pn * HALF + wc * 32 + 8 * fq; const PG8_LAS float* rsr = rsl + rl0;
; #pragma unroll
;         for (int ai = 0; ai < 2; ++ai) { if (ai == 1 && u.half != 0) break;
; #pragma unroll
;             for (int m = 0; m < 4; ++m) { const float rf = rsr[ai * HALF + m * 16]; f32x4 v0 = acc[ai][0][m][0] * rf, v1 = acc[ai][0][m][1] * rf; const f32x4 u0 = acc[ai][1][m][0] * rf, u1 = acc[ai][1][m][1] * rf;
; #pragma unroll
;                 for (int e = 0; e < 4; ++e) { v0[e] = v0[e] * sigm(v0[e]) * u0[e]; v1[e] = v1[e] * sigm(v1[e]) * u1[e]; }
;                 *(u32x4*)(H + (size_t)(row0 + ai * HALF + m * 16) * DFF + col0) = pack8(v0, v1); } }
;     }
.LBB0_1480:
	ds_read_b32 v236, v148
	v_lshl_or_b32 v244, s20, 7, v149
	v_lshl_add_u32 v228, s14, 8, v146
	v_ashrrev_i32_e32 v245, 31, v244
	v_mov_b64_e32 v[240:241], s[4:5]
	v_mad_i64_i32 v[240:241], s[0:1], v228, s2, v[240:241]
	v_lshlrev_b64 v[244:245], 1, v[244:245]
	v_lshl_add_u64 v[240:241], v[240:241], 0, v[244:245]
	s_waitcnt lgkmcnt(0)
	ds_read_b32 v239, v148 offset:64
	v_mul_f32_e32 v237, 0xbfb8aa3b, v236
	v_mul_f32_e32 v238, v236, v236
	v_rcp_f32_e32 v238, v238
	v_mul_f32_e32 v228, v237, v128
	v_mul_f32_e32 v229, v237, v129
	v_mul_f32_e32 v230, v237, v130
	v_mul_f32_e32 v231, v237, v131
	v_mul_f32_e32 v232, v237, v124
	v_mul_f32_e32 v233, v237, v125
	v_mul_f32_e32 v234, v237, v126
	v_mul_f32_e32 v235, v237, v127
	v_exp_f32_e32 v228, v228
	v_exp_f32_e32 v229, v229
	v_exp_f32_e32 v230, v230
	v_exp_f32_e32 v231, v231
	v_exp_f32_e32 v232, v232
	v_exp_f32_e32 v233, v233
	v_exp_f32_e32 v234, v234
	v_exp_f32_e32 v235, v235
	v_fma_f32 v228, v228, v238, v238
	v_fma_f32 v229, v229, v238, v238
	v_fma_f32 v230, v230, v238, v238
	v_fma_f32 v231, v231, v238, v238
	v_fma_f32 v232, v232, v238, v238
	v_fma_f32 v233, v233, v238, v238
	v_fma_f32 v234, v234, v238, v238
	v_fma_f32 v235, v235, v238, v238
	v_rcp_f32_e32 v228, v228
	v_rcp_f32_e32 v229, v229
	v_rcp_f32_e32 v230, v230
	v_rcp_f32_e32 v231, v231
	v_rcp_f32_e32 v232, v232
	v_rcp_f32_e32 v233, v233
	v_rcp_f32_e32 v234, v234
	v_rcp_f32_e32 v235, v235
	v_mul_f32_e32 v120, v128, v120
	v_mul_f32_e32 v121, v129, v121
	v_mul_f32_e32 v122, v130, v122
	v_mul_f32_e32 v123, v131, v123
	v_mul_f32_e32 v116, v124, v116
	v_mul_f32_e32 v117, v125, v117
	v_mul_f32_e32 v118, v126, v118
	v_mul_f32_e32 v119, v127, v119
	v_mul_f32_e32 v128, v120, v228
	v_mul_f32_e32 v129, v121, v229
	v_mul_f32_e32 v130, v122, v230
	v_mul_f32_e32 v131, v123, v231
	v_mul_f32_e32 v124, v116, v232
	v_mul_f32_e32 v125, v117, v233
	v_mul_f32_e32 v126, v118, v234
	v_mul_f32_e32 v127, v119, v235
	v_cvt_pk_bf16_f32 v128, v128, v129
	v_cvt_pk_bf16_f32 v129, v130, v131
	v_cvt_pk_bf16_f32 v130, v124, v125
	v_cvt_pk_bf16_f32 v131, v126, v127
	global_store_dwordx4 v[240:241], v[128:131], off
	s_waitcnt lgkmcnt(0)
	v_mov_b32_e32 v236, v239
	ds_read_b32 v239, v148 offset:128
	v_mul_f32_e32 v237, 0xbfb8aa3b, v236
	v_mul_f32_e32 v238, v236, v236
	v_rcp_f32_e32 v238, v238
	v_mul_f32_e32 v228, v237, v112
	v_mul_f32_e32 v229, v237, v113
	v_mul_f32_e32 v230, v237, v114
	v_mul_f32_e32 v231, v237, v115
	v_mul_f32_e32 v232, v237, v108
	v_mul_f32_e32 v233, v237, v109
	v_mul_f32_e32 v234, v237, v110
	v_mul_f32_e32 v235, v237, v111
	v_exp_f32_e32 v228, v228
	v_exp_f32_e32 v229, v229
	v_exp_f32_e32 v230, v230
	v_exp_f32_e32 v231, v231
	v_exp_f32_e32 v232, v232
	v_exp_f32_e32 v233, v233
	v_exp_f32_e32 v234, v234
	v_exp_f32_e32 v235, v235
	v_fma_f32 v228, v228, v238, v238
	v_fma_f32 v229, v229, v238, v238
	v_fma_f32 v230, v230, v238, v238
	v_fma_f32 v231, v231, v238, v238
	v_fma_f32 v232, v232, v238, v238
	v_fma_f32 v233, v233, v238, v238
	v_fma_f32 v234, v234, v238, v238
	v_fma_f32 v235, v235, v238, v238
	v_rcp_f32_e32 v228, v228
	v_rcp_f32_e32 v229, v229
	v_rcp_f32_e32 v230, v230
	v_rcp_f32_e32 v231, v231
	v_rcp_f32_e32 v232, v232
	v_rcp_f32_e32 v233, v233
	v_rcp_f32_e32 v234, v234
	v_rcp_f32_e32 v235, v235
	v_mul_f32_e32 v104, v112, v104
	v_mul_f32_e32 v105, v113, v105
	v_mul_f32_e32 v106, v114, v106
	v_mul_f32_e32 v107, v115, v107
	v_mul_f32_e32 v100, v108, v100
	v_mul_f32_e32 v101, v109, v101
	v_mul_f32_e32 v102, v110, v102
	v_mul_f32_e32 v103, v111, v103
	s_mov_b64 s[0:1], 0x16000
	v_lshl_add_u64 v[242:243], v[240:241], 0, s[0:1]
	v_mul_f32_e32 v112, v104, v228
	v_mul_f32_e32 v113, v105, v229
	v_mul_f32_e32 v114, v106, v230
	v_mul_f32_e32 v115, v107, v231
	v_mul_f32_e32 v108, v100, v232
	v_mul_f32_e32 v109, v101, v233
	v_mul_f32_e32 v110, v102, v234
	v_mul_f32_e32 v111, v103, v235
	v_cvt_pk_bf16_f32 v112, v112, v113
	v_cvt_pk_bf16_f32 v113, v114, v115
	v_cvt_pk_bf16_f32 v114, v108, v109
	v_cvt_pk_bf16_f32 v115, v110, v111
	global_store_dwordx4 v[242:243], v[112:115], off
	s_waitcnt lgkmcnt(0)
	v_mov_b32_e32 v236, v239
	ds_read_b32 v239, v148 offset:192
	v_mul_f32_e32 v237, 0xbfb8aa3b, v236
	v_mul_f32_e32 v238, v236, v236
	v_rcp_f32_e32 v238, v238
	v_mul_f32_e32 v228, v237, v96
	v_mul_f32_e32 v229, v237, v97
	v_mul_f32_e32 v230, v237, v98
	v_mul_f32_e32 v231, v237, v99
	v_mul_f32_e32 v232, v237, v92
	v_mul_f32_e32 v233, v237, v93
	v_mul_f32_e32 v234, v237, v94
	v_mul_f32_e32 v235, v237, v95
	v_exp_f32_e32 v228, v228
	v_exp_f32_e32 v229, v229
	v_exp_f32_e32 v230, v230
	v_exp_f32_e32 v231, v231
	v_exp_f32_e32 v232, v232
	v_exp_f32_e32 v233, v233
	v_exp_f32_e32 v234, v234
	v_exp_f32_e32 v235, v235
	v_fma_f32 v228, v228, v238, v238
	v_fma_f32 v229, v229, v238, v238
	v_fma_f32 v230, v230, v238, v238
	v_fma_f32 v231, v231, v238, v238
	v_fma_f32 v232, v232, v238, v238
	v_fma_f32 v233, v233, v238, v238
	v_fma_f32 v234, v234, v238, v238
	v_fma_f32 v235, v235, v238, v238
	v_rcp_f32_e32 v228, v228
	v_rcp_f32_e32 v229, v229
	v_rcp_f32_e32 v230, v230
	v_rcp_f32_e32 v231, v231
	v_rcp_f32_e32 v232, v232
	v_rcp_f32_e32 v233, v233
	v_rcp_f32_e32 v234, v234
	v_rcp_f32_e32 v235, v235
	v_mul_f32_e32 v88, v96, v88
	v_mul_f32_e32 v89, v97, v89
	v_mul_f32_e32 v90, v98, v90
	v_mul_f32_e32 v91, v99, v91
	v_mul_f32_e32 v84, v92, v84
	v_mul_f32_e32 v85, v93, v85
	v_mul_f32_e32 v86, v94, v86
	v_mul_f32_e32 v87, v95, v87
	s_mov_b64 s[0:1], 0x2c000
	v_lshl_add_u64 v[242:243], v[240:241], 0, s[0:1]
	v_mul_f32_e32 v96, v88, v228
	v_mul_f32_e32 v97, v89, v229
	v_mul_f32_e32 v98, v90, v230
	v_mul_f32_e32 v99, v91, v231
	v_mul_f32_e32 v92, v84, v232
	v_mul_f32_e32 v93, v85, v233
	v_mul_f32_e32 v94, v86, v234
	v_mul_f32_e32 v95, v87, v235
	v_cvt_pk_bf16_f32 v96, v96, v97
	v_cvt_pk_bf16_f32 v97, v98, v99
	v_cvt_pk_bf16_f32 v98, v92, v93
	v_cvt_pk_bf16_f32 v99, v94, v95
	global_store_dwordx4 v[242:243], v[96:99], off
	s_waitcnt lgkmcnt(0)
; #define PG8_LAS __attribute__((address_space(3)))
; __device__ __forceinline__ float sigm(float x) { return __builtin_amdgcn_rcpf(1.0f + __builtin_amdgcn_exp2f(-1.4426950408889634f * x)); }
; __device__ __forceinline__ u32x4 pack8(const f32x4 a, const f32x4 b) { u32x4 w; w.x = cvt_pk_bf16(a[0], a[1]); w.y = cvt_pk_bf16(a[2], a[3]); w.z = cvt_pk_bf16(b[0], b[1]); w.w = cvt_pk_bf16(b[2], b[3]); return w; }
;     __device__ __forceinline__ void operator()(const f32x4 (&acc)[2][2][4][2], const Unit& u, int wr, int wc, int fr, int fq) const {
;         const int rl0 = wr * 64 + fr + (u.half == 2 ? HALF : 0), row0 = u.pm * BM + rl0, col0 = u.pn * HALF + wc * 32 + 8 * fq; const PG8_LAS float* rsr = rsl + rl0;
; #pragma unroll
;         for (int ai = 0; ai < 2; ++ai) { if (ai == 1 && u.half != 0) break;
; #pragma unroll
;             for (int m = 0; m < 4; ++m) { const float rf = rsr[ai * HALF + m * 16]; f32x4 v0 = acc[ai][0][m][0] * rf, v1 = acc[ai][0][m][1] * rf; const f32x4 u0 = acc[ai][1][m][0] * rf, u1 = acc[ai][1][m][1] * rf;
; #pragma unroll
;                 for (int e = 0; e < 4; ++e) { v0[e] = v0[e] * sigm(v0[e]) * u0[e]; v1[e] = v1[e] * sigm(v1[e]) * u1[e]; }
;                 *(u32x4*)(H + (size_t)(row0 + ai * HALF + m * 16) * DFF + col0) = pack8(v0, v1); } }
;     }
	v_mov_b32_e32 v236, v239
	ds_read_b32 v239, v148 offset:512
	v_mul_f32_e32 v237, 0xbfb8aa3b, v236
	v_mul_f32_e32 v238, v236, v236
	v_rcp_f32_e32 v238, v238
	v_mul_f32_e32 v228, v237, v80
	v_mul_f32_e32 v229, v237, v81
	v_mul_f32_e32 v230, v237, v82
	v_mul_f32_e32 v231, v237, v83
	v_mul_f32_e32 v232, v237, v76
	v_mul_f32_e32 v233, v237, v77
	v_mul_f32_e32 v234, v237, v78
	v_mul_f32_e32 v235, v237, v79
	v_exp_f32_e32 v228, v228
	v_exp_f32_e32 v229, v229
	v_exp_f32_e32 v230, v230
	v_exp_f32_e32 v231, v231
	v_exp_f32_e32 v232, v232
	v_exp_f32_e32 v233, v233
	v_exp_f32_e32 v234, v234
	v_exp_f32_e32 v235, v235
	v_fma_f32 v228, v228, v238, v238
	v_fma_f32 v229, v229, v238, v238
	v_fma_f32 v230, v230, v238, v238
	v_fma_f32 v231, v231, v238, v238
	v_fma_f32 v232, v232, v238, v238
	v_fma_f32 v233, v233, v238, v238
	v_fma_f32 v234, v234, v238, v238
	v_fma_f32 v235, v235, v238, v238
	v_rcp_f32_e32 v228, v228
	v_rcp_f32_e32 v229, v229
	v_rcp_f32_e32 v230, v230
	v_rcp_f32_e32 v231, v231
	v_rcp_f32_e32 v232, v232
	v_rcp_f32_e32 v233, v233
	v_rcp_f32_e32 v234, v234
	v_rcp_f32_e32 v235, v235
	v_mul_f32_e32 v72, v80, v72
	v_mul_f32_e32 v73, v81, v73
	v_mul_f32_e32 v74, v82, v74
	v_mul_f32_e32 v75, v83, v75
	v_mul_f32_e32 v68, v76, v68
	v_mul_f32_e32 v69, v77, v69
	v_mul_f32_e32 v70, v78, v70
	v_mul_f32_e32 v71, v79, v71
	s_mov_b64 s[0:1], 0x42000
	v_lshl_add_u64 v[242:243], v[240:241], 0, s[0:1]
	v_mul_f32_e32 v80, v72, v228
	v_mul_f32_e32 v81, v73, v229
	v_mul_f32_e32 v82, v74, v230
	v_mul_f32_e32 v83, v75, v231
	v_mul_f32_e32 v76, v68, v232
	v_mul_f32_e32 v77, v69, v233
	v_mul_f32_e32 v78, v70, v234
	v_mul_f32_e32 v79, v71, v235
	v_cvt_pk_bf16_f32 v80, v80, v81
	v_cvt_pk_bf16_f32 v81, v82, v83
	v_cvt_pk_bf16_f32 v82, v76, v77
	v_cvt_pk_bf16_f32 v83, v78, v79
	global_store_dwordx4 v[242:243], v[80:83], off
	s_waitcnt lgkmcnt(0)
	v_mov_b32_e32 v236, v239
	ds_read_b32 v239, v148 offset:576
	v_mul_f32_e32 v237, 0xbfb8aa3b, v236
	v_mul_f32_e32 v238, v236, v236
	v_rcp_f32_e32 v238, v238
	v_mul_f32_e32 v228, v237, v64
	v_mul_f32_e32 v229, v237, v65
	v_mul_f32_e32 v230, v237, v66
	v_mul_f32_e32 v231, v237, v67
	v_mul_f32_e32 v232, v237, v60
	v_mul_f32_e32 v233, v237, v61
	v_mul_f32_e32 v234, v237, v62
	v_mul_f32_e32 v235, v237, v63
	v_exp_f32_e32 v228, v228
	v_exp_f32_e32 v229, v229
	v_exp_f32_e32 v230, v230
	v_exp_f32_e32 v231, v231
	v_exp_f32_e32 v232, v232
	v_exp_f32_e32 v233, v233
	v_exp_f32_e32 v234, v234
	v_exp_f32_e32 v235, v235
	v_fma_f32 v228, v228, v238, v238
	v_fma_f32 v229, v229, v238, v238
	v_fma_f32 v230, v230, v238, v238
	v_fma_f32 v231, v231, v238, v238
	v_fma_f32 v232, v232, v238, v238
	v_fma_f32 v233, v233, v238, v238
	v_fma_f32 v234, v234, v238, v238
	v_fma_f32 v235, v235, v238, v238
	v_rcp_f32_e32 v228, v228
	v_rcp_f32_e32 v229, v229
	v_rcp_f32_e32 v230, v230
	v_rcp_f32_e32 v231, v231
	v_rcp_f32_e32 v232, v232
	v_rcp_f32_e32 v233, v233
	v_rcp_f32_e32 v234, v234
	v_rcp_f32_e32 v235, v235
	v_mul_f32_e32 v56, v64, v56
	v_mul_f32_e32 v57, v65, v57
	v_mul_f32_e32 v58, v66, v58
	v_mul_f32_e32 v59, v67, v59
	v_mul_f32_e32 v52, v60, v52
	v_mul_f32_e32 v53, v61, v53
	v_mul_f32_e32 v54, v62, v54
	v_mul_f32_e32 v55, v63, v55
	s_mov_b64 s[0:1], 0xb0000
	v_lshl_add_u64 v[242:243], v[240:241], 0, s[0:1]
	v_mul_f32_e32 v64, v56, v228
	v_mul_f32_e32 v65, v57, v229
	v_mul_f32_e32 v66, v58, v230
	v_mul_f32_e32 v67, v59, v231
	v_mul_f32_e32 v60, v52, v232
	v_mul_f32_e32 v61, v53, v233
	v_mul_f32_e32 v62, v54, v234
	v_mul_f32_e32 v63, v55, v235
	v_cvt_pk_bf16_f32 v64, v64, v65
	v_cvt_pk_bf16_f32 v65, v66, v67
	v_cvt_pk_bf16_f32 v66, v60, v61
	v_cvt_pk_bf16_f32 v67, v62, v63
	global_store_dwordx4 v[242:243], v[64:67], off
	s_waitcnt lgkmcnt(0)
	v_mov_b32_e32 v236, v239
	ds_read_b32 v239, v148 offset:640
	v_mul_f32_e32 v237, 0xbfb8aa3b, v236
	v_mul_f32_e32 v238, v236, v236
	v_rcp_f32_e32 v238, v238
	v_mul_f32_e32 v228, v237, v48
	v_mul_f32_e32 v229, v237, v49
	v_mul_f32_e32 v230, v237, v50
	v_mul_f32_e32 v231, v237, v51
	v_mul_f32_e32 v232, v237, v44
	v_mul_f32_e32 v233, v237, v45
	v_mul_f32_e32 v234, v237, v46
	v_mul_f32_e32 v235, v237, v47
	v_exp_f32_e32 v228, v228
	v_exp_f32_e32 v229, v229
	v_exp_f32_e32 v230, v230
	v_exp_f32_e32 v231, v231
	v_exp_f32_e32 v232, v232
	v_exp_f32_e32 v233, v233
	v_exp_f32_e32 v234, v234
	v_exp_f32_e32 v235, v235
	v_fma_f32 v228, v228, v238, v238
	v_fma_f32 v229, v229, v238, v238
	v_fma_f32 v230, v230, v238, v238
	v_fma_f32 v231, v231, v238, v238
	v_fma_f32 v232, v232, v238, v238
	v_fma_f32 v233, v233, v238, v238
	v_fma_f32 v234, v234, v238, v238
	v_fma_f32 v235, v235, v238, v238
	v_rcp_f32_e32 v228, v228
	v_rcp_f32_e32 v229, v229
	v_rcp_f32_e32 v230, v230
	v_rcp_f32_e32 v231, v231
	v_rcp_f32_e32 v232, v232
	v_rcp_f32_e32 v233, v233
	v_rcp_f32_e32 v234, v234
	v_rcp_f32_e32 v235, v235
	v_mul_f32_e32 v40, v48, v40
	v_mul_f32_e32 v41, v49, v41
	v_mul_f32_e32 v42, v50, v42
	v_mul_f32_e32 v43, v51, v43
	v_mul_f32_e32 v36, v44, v36
	v_mul_f32_e32 v37, v45, v37
	v_mul_f32_e32 v38, v46, v38
	v_mul_f32_e32 v39, v47, v39
	s_mov_b64 s[0:1], 0xc6000
	v_lshl_add_u64 v[242:243], v[240:241], 0, s[0:1]
	v_mul_f32_e32 v48, v40, v228
	v_mul_f32_e32 v49, v41, v229
	v_mul_f32_e32 v50, v42, v230
	v_mul_f32_e32 v51, v43, v231
	v_mul_f32_e32 v44, v36, v232
	v_mul_f32_e32 v45, v37, v233
	v_mul_f32_e32 v46, v38, v234
	v_mul_f32_e32 v47, v39, v235
	v_cvt_pk_bf16_f32 v48, v48, v49
	v_cvt_pk_bf16_f32 v49, v50, v51
	v_cvt_pk_bf16_f32 v50, v44, v45
	v_cvt_pk_bf16_f32 v51, v46, v47
	global_store_dwordx4 v[242:243], v[48:51], off
	s_waitcnt lgkmcnt(0)
; #define PG8_LAS __attribute__((address_space(3)))
; __device__ __forceinline__ float sigm(float x) { return __builtin_amdgcn_rcpf(1.0f + __builtin_amdgcn_exp2f(-1.4426950408889634f * x)); }
; __device__ __forceinline__ u32x4 pack8(const f32x4 a, const f32x4 b) { u32x4 w; w.x = cvt_pk_bf16(a[0], a[1]); w.y = cvt_pk_bf16(a[2], a[3]); w.z = cvt_pk_bf16(b[0], b[1]); w.w = cvt_pk_bf16(b[2], b[3]); return w; }
; #define PG8_BAR __builtin_amdgcn_s_barrier()
;     __device__ __forceinline__ void operator()(const f32x4 (&acc)[2][2][4][2], const Unit& u, int wr, int wc, int fr, int fq) const {
;         const int rl0 = wr * 64 + fr + (u.half == 2 ? HALF : 0), row0 = u.pm * BM + rl0, col0 = u.pn * HALF + wc * 32 + 8 * fq; const PG8_LAS float* rsr = rsl + rl0;
; #pragma unroll
;         for (int ai = 0; ai < 2; ++ai) { if (ai == 1 && u.half != 0) break;
; #pragma unroll
;             for (int m = 0; m < 4; ++m) { const float rf = rsr[ai * HALF + m * 16]; f32x4 v0 = acc[ai][0][m][0] * rf, v1 = acc[ai][0][m][1] * rf; const f32x4 u0 = acc[ai][1][m][0] * rf, u1 = acc[ai][1][m][1] * rf;
; #pragma unroll
;                 for (int e = 0; e < 4; ++e) { v0[e] = v0[e] * sigm(v0[e]) * u0[e]; v1[e] = v1[e] * sigm(v1[e]) * u1[e]; }
;                 *(u32x4*)(H + (size_t)(row0 + ai * HALF + m * 16) * DFF + col0) = pack8(v0, v1); } }
;     }
; template <class Epi, class Sched, bool ALIGN_EPI = false, bool SP2 = false>
; __device__ __forceinline__ void gemm_phase(PG8_LAS unsigned char* lds, const Gemm g, const Sched& S, const Epi& E) {
;     ...
;         if (!has_next) break;
;         if constexpr (!Epi::CHAIN) {
; #pragma unroll
;         for (int a = 0; a < 2; ++a)
; #pragma unroll
;             for (int b = 0; b < 2; ++b)
; #pragma unroll
;                 for (int m = 0; m < 4; ++m)
; #pragma unroll
;                     for (int n = 0; n < 2; ++n) acc[a][b][m][n] = (f32x4){0.f, 0.f, 0.f, 0.f};
;         }
;         cur = nxt; cA = nA; cB = nB; ++ui;
;         if constexpr (ALIGN_EPI) { if (wr == 1) PG8_BAR; }
	v_mov_b32_e32 v236, v239
	ds_read_b32 v239, v148 offset:704
	v_mul_f32_e32 v237, 0xbfb8aa3b, v236
	v_mul_f32_e32 v238, v236, v236
	v_rcp_f32_e32 v238, v238
	v_mul_f32_e32 v228, v237, v32
	v_mul_f32_e32 v229, v237, v33
	v_mul_f32_e32 v230, v237, v34
	v_mul_f32_e32 v231, v237, v35
	v_mul_f32_e32 v232, v237, v28
	v_mul_f32_e32 v233, v237, v29
	v_mul_f32_e32 v234, v237, v30
	v_mul_f32_e32 v235, v237, v31
	v_exp_f32_e32 v228, v228
	v_exp_f32_e32 v229, v229
	v_exp_f32_e32 v230, v230
	v_exp_f32_e32 v231, v231
	v_exp_f32_e32 v232, v232
	v_exp_f32_e32 v233, v233
	v_exp_f32_e32 v234, v234
	v_exp_f32_e32 v235, v235
	v_fma_f32 v228, v228, v238, v238
	v_fma_f32 v229, v229, v238, v238
	v_fma_f32 v230, v230, v238, v238
	v_fma_f32 v231, v231, v238, v238
	v_fma_f32 v232, v232, v238, v238
	v_fma_f32 v233, v233, v238, v238
	v_fma_f32 v234, v234, v238, v238
	v_fma_f32 v235, v235, v238, v238
	v_rcp_f32_e32 v228, v228
	v_rcp_f32_e32 v229, v229
	v_rcp_f32_e32 v230, v230
	v_rcp_f32_e32 v231, v231
	v_rcp_f32_e32 v232, v232
	v_rcp_f32_e32 v233, v233
	v_rcp_f32_e32 v234, v234
	v_rcp_f32_e32 v235, v235
	v_mul_f32_e32 v24, v32, v24
	v_mul_f32_e32 v25, v33, v25
	v_mul_f32_e32 v26, v34, v26
	v_mul_f32_e32 v27, v35, v27
	v_mul_f32_e32 v20, v28, v20
	v_mul_f32_e32 v21, v29, v21
	v_mul_f32_e32 v22, v30, v22
	v_mul_f32_e32 v23, v31, v23
	s_mov_b64 s[0:1], 0xdc000
	v_lshl_add_u64 v[242:243], v[240:241], 0, s[0:1]
	v_mul_f32_e32 v32, v24, v228
	v_mul_f32_e32 v33, v25, v229
	v_mul_f32_e32 v34, v26, v230
	v_mul_f32_e32 v35, v27, v231
	v_mul_f32_e32 v28, v20, v232
	v_mul_f32_e32 v29, v21, v233
	v_mul_f32_e32 v30, v22, v234
	v_mul_f32_e32 v31, v23, v235
	v_cvt_pk_bf16_f32 v32, v32, v33
	v_cvt_pk_bf16_f32 v33, v34, v35
	v_cvt_pk_bf16_f32 v34, v28, v29
	v_cvt_pk_bf16_f32 v35, v30, v31
	global_store_dwordx4 v[242:243], v[32:35], off
	s_waitcnt lgkmcnt(0)
	v_mov_b32_e32 v236, v239
	v_mul_f32_e32 v237, 0xbfb8aa3b, v236
	v_mul_f32_e32 v238, v236, v236
	v_rcp_f32_e32 v238, v238
	v_mul_f32_e32 v228, v237, v16
	v_mul_f32_e32 v229, v237, v17
	v_mul_f32_e32 v230, v237, v18
	v_mul_f32_e32 v231, v237, v19
	v_mul_f32_e32 v232, v237, v12
	v_mul_f32_e32 v233, v237, v13
	v_mul_f32_e32 v234, v237, v14
	v_mul_f32_e32 v235, v237, v15
	v_exp_f32_e32 v228, v228
	v_exp_f32_e32 v229, v229
	v_exp_f32_e32 v230, v230
	v_exp_f32_e32 v231, v231
	v_exp_f32_e32 v232, v232
	v_exp_f32_e32 v233, v233
	v_exp_f32_e32 v234, v234
	v_exp_f32_e32 v235, v235
	v_fma_f32 v228, v228, v238, v238
	v_fma_f32 v229, v229, v238, v238
	v_fma_f32 v230, v230, v238, v238
	v_fma_f32 v231, v231, v238, v238
	v_fma_f32 v232, v232, v238, v238
	v_fma_f32 v233, v233, v238, v238
	v_fma_f32 v234, v234, v238, v238
	v_fma_f32 v235, v235, v238, v238
	v_rcp_f32_e32 v228, v228
	v_rcp_f32_e32 v229, v229
	v_rcp_f32_e32 v230, v230
	v_rcp_f32_e32 v231, v231
	v_rcp_f32_e32 v232, v232
	v_rcp_f32_e32 v233, v233
	v_rcp_f32_e32 v234, v234
	v_rcp_f32_e32 v235, v235
	v_mul_f32_e32 v8, v16, v8
	v_mul_f32_e32 v9, v17, v9
	v_mul_f32_e32 v10, v18, v10
	v_mul_f32_e32 v11, v19, v11
	v_mul_f32_e32 v4, v12, v4
	v_mul_f32_e32 v5, v13, v5
	v_mul_f32_e32 v6, v14, v6
	v_mul_f32_e32 v7, v15, v7
	s_mov_b64 s[0:1], 0xf2000
	v_lshl_add_u64 v[242:243], v[240:241], 0, s[0:1]
	v_mul_f32_e32 v16, v8, v228
	v_mul_f32_e32 v17, v9, v229
	v_mul_f32_e32 v18, v10, v230
	v_mul_f32_e32 v19, v11, v231
	v_mul_f32_e32 v12, v4, v232
	v_mul_f32_e32 v13, v5, v233
	v_mul_f32_e32 v14, v6, v234
	v_mul_f32_e32 v15, v7, v235
	v_cvt_pk_bf16_f32 v16, v16, v17
	v_cvt_pk_bf16_f32 v17, v18, v19
	v_cvt_pk_bf16_f32 v18, v12, v13
	v_cvt_pk_bf16_f32 v19, v14, v15
	global_store_dwordx4 v[242:243], v[16:19], off
	s_andn2_b64 vcc, exec, s[38:39]
	s_mov_b64 s[0:1], -1
	s_cbranch_vccnz .LBB0_1473
	s_andn2_b64 vcc, exec, s[8:9]
	s_cbranch_vccnz .LBB0_1472
	s_barrier
	s_branch .LBB0_1472
